# v24 + P2 conversion share rebalanced: common part 11*2048 items, remainder to the 9-unit workgroups
# speedup vs baseline: 1.0086x; 1.0085x over previous
.LBB0_219:
	s_cmp_lt_i32 s42, s33
	s_cselect_b64 s[14:15], -1, 0
	s_cmp_ge_i32 s42, s33
	s_cselect_b64 s[8:9], -1, 0
	s_add_u32 s40, s50, 0xd200000
	s_addc_u32 s41, s51, 0
	s_and_b64 vcc, exec, s[8:9]
	s_cbranch_vccnz .LBB0_330
	s_lshl_b32 s0, s86, 3
	s_add_i32 s63, s0, s88
	s_cmp_gt_i32 s63, 0x57ff
	s_waitcnt vmcnt(0)
	s_barrier
	s_cbranch_scc1 .LBB0_329
	s_ashr_i32 s0, s63, 9
	s_mulk_i32 s0, 0x300
	s_and_b32 s22, s63, 0x1ff
	s_add_i32 s23, s0, s22
	s_addk_i32 s23, 0x3000
	s_cmpk_gt_i32 s23, 0x25ff
	s_cbranch_scc0 .LBB0_228
	s_cmpk_gt_u32 s23, 0x27ff
	s_cbranch_scc0 .LBB0_229
	s_cmpk_gt_u32 s23, 0x2bff
	s_cbranch_scc0 .LBB0_230
	s_cmpk_gt_u32 s23, 0x2fff
	s_cbranch_scc0 .LBB0_231
	s_add_i32 s24, s23, 0xffffd000
	s_and_b32 s0, s24, 0xffff
	s_mul_i32 s0, s0, 0xaaab
	s_lshr_b32 s20, s0, 25
	s_mul_i32 s0, s20, 0x300
	s_sub_i32 s0, s24, s0
	s_and_b32 s21, s0, 0xffff
	s_cmpk_gt_u32 s21, 0x1ff
	s_cbranch_scc0 .LBB0_232
	s_cmpk_gt_u32 s24, 0xbfff
	s_cbranch_scc0 .LBB0_233
	s_add_i32 s0, 0, 0x27ea8
	v_mov_b32_e32 v2, s0
	ds_read_b64 v[2:3], v2
	s_mov_b64 s[16:17], 0
	s_waitcnt lgkmcnt(0)
	v_readfirstlane_b32 s0, v2
	v_readfirstlane_b32 s1, v3
	s_branch .LBB0_234

.LBB0_258:
	s_waitcnt lgkmcnt(0)
	s_add_i32 s63, s64, s27
	s_cmp_gt_i32 s63, 0x57ff
	s_cselect_b64 s[18:19], -1, 0

.LBB0_260:
	s_add_i32 s64, s63, s27
	s_cmp_lt_i32 s64, 0x5800
	s_cselect_b64 s[18:19], -1, 0
	s_cmp_gt_i32 s64, 0x57ff
	s_cbranch_scc1 .LBB0_289
	s_ashr_i32 s16, s64, 9
	s_mulk_i32 s16, 0x300
	s_and_b32 s67, s64, 0x1ff
	s_add_i32 s68, s16, s67
	s_addk_i32 s68, 0x3000
	s_cmpk_gt_i32 s68, 0x25ff
	s_mov_b64 s[24:25], -1
	s_cbranch_scc0 .LBB0_286
	s_cmpk_gt_u32 s68, 0x27ff
	s_cbranch_scc0 .LBB0_283
	s_cmpk_gt_u32 s68, 0x2bff
	s_cbranch_scc0 .LBB0_280
	s_cmpk_gt_u32 s68, 0x2fff
	s_cbranch_scc0 .LBB0_277
	s_add_i32 s65, s68, 0xffffd000
	s_and_b32 s16, s65, 0xffff
	s_mul_i32 s16, s16, 0xaaab
	s_lshr_b32 s24, s16, 25
	s_mul_i32 s16, s24, 0x300
	s_sub_i32 s16, s65, s16
	s_and_b32 s25, s16, 0xffff
	s_cmpk_gt_u32 s25, 0x1ff
	s_mov_b64 s[22:23], -1
	s_cbranch_scc0 .LBB0_271
	s_cmpk_gt_u32 s65, 0xbfff
	s_mov_b64 s[20:21], -1
	s_cbranch_scc0 .LBB0_268
	v_mov_b32_e32 v58, s54
	ds_read_b64 v[58:59], v58
	s_mov_b64 s[20:21], 0
	s_waitcnt lgkmcnt(0)
	v_readfirstlane_b32 s16, v58
	v_readfirstlane_b32 s17, v59

.LBB0_292:
	s_waitcnt lgkmcnt(0)
	s_andn2_b64 vcc, exec, s[18:19]
	s_mov_b64 s[18:19], -1
	s_cbranch_vccnz .LBB0_259
	s_add_i32 s67, s53, s63
	s_cmp_gt_i32 s67, 0x57ff
	s_cbranch_scc1 .LBB0_326
	s_ashr_i32 s0, s67, 9
	s_mulk_i32 s0, 0x300
	s_and_b32 s24, s67, 0x1ff
	s_add_i32 s25, s0, s24
	s_addk_i32 s25, 0x3000
	s_cmpk_gt_i32 s25, 0x25ff
	s_mov_b64 s[22:23], -1
	s_cbranch_scc0 .LBB0_323
	s_cmpk_gt_u32 s25, 0x27ff
	s_cbranch_scc0 .LBB0_320
	s_cmpk_gt_u32 s25, 0x2bff
	s_cbranch_scc0 .LBB0_317
	s_cmpk_gt_u32 s25, 0x2fff
	s_cbranch_scc0 .LBB0_314
	s_add_i32 s26, s25, 0xffffd000
	s_and_b32 s0, s26, 0xffff
	s_mul_i32 s0, s0, 0xaaab
	s_lshr_b32 s22, s0, 25
	s_mul_i32 s0, s22, 0x300
	s_sub_i32 s0, s26, s0
	s_and_b32 s23, s0, 0xffff
	s_cmpk_gt_u32 s23, 0x1ff
	s_mov_b64 s[20:21], -1
	s_cbranch_scc0 .LBB0_304
	s_cmpk_gt_u32 s26, 0xbfff
	s_mov_b64 s[18:19], -1
	s_cbranch_scc0 .LBB0_301
	v_mov_b32_e32 v2, s54
	ds_read_b64 v[2:3], v2
	s_mov_b64 s[18:19], 0
	s_waitcnt lgkmcnt(0)
	v_readfirstlane_b32 s0, v2
	v_readfirstlane_b32 s1, v3

.LBB0_376:
	s_andn2_b64 vcc, exec, s[8:9]
	s_cbranch_vccnz .LBB0_599
	s_cmpk_eq_i32 s52, 0x100
	s_cselect_b64 s[0:1], -1, 0
	s_movk_i32 s10, 0x5800
	s_and_b64 s[8:9], s[0:1], exec
	s_cselect_b32 s21, s10, 0x8200
	s_lshl_b32 s8, s86, 3
	s_add_i32 s57, s8, s88
	s_mul_i32 s8, s88, 0x4100
	s_add_i32 s20, s8, 0
	s_cmp_ge_i32 s57, s21
	s_waitcnt vmcnt(0)
	s_barrier
	s_cbranch_scc1 .LBB0_486
	s_ashr_i32 s8, s57, 9
	s_mulk_i32 s8, 0x300
	s_and_b32 s16, s57, 0x1ff
	s_add_i32 s17, s8, s16
	s_addk_i32 s17, 0x3000
	s_cmpk_gt_i32 s17, 0x25ff
	s_cbranch_scc0 .LBB0_385
	s_cmpk_gt_u32 s17, 0x27ff
	s_cbranch_scc0 .LBB0_386
	s_cmpk_gt_u32 s17, 0x2bff
	s_cbranch_scc0 .LBB0_387
	s_cmpk_gt_u32 s17, 0x2fff
	s_cbranch_scc0 .LBB0_388
	s_add_i32 s18, s17, 0xffffd000
	s_and_b32 s8, s18, 0xffff
	s_mul_i32 s8, s8, 0xaaab
	s_lshr_b32 s14, s8, 25
	s_mul_i32 s8, s14, 0x300
	s_sub_i32 s8, s18, s8
	s_and_b32 s15, s8, 0xffff
	s_cmpk_gt_u32 s15, 0x1ff
	s_cbranch_scc0 .LBB0_389
	s_cmpk_gt_u32 s18, 0xbfff
	s_cbranch_scc0 .LBB0_390
	s_add_i32 s8, 0, 0x27ea8
	v_mov_b32_e32 v2, s8
	ds_read_b64 v[2:3], v2
	s_mov_b64 s[10:11], 0
	s_waitcnt lgkmcnt(0)
	v_readfirstlane_b32 s8, v2
	v_readfirstlane_b32 s9, v3
	s_branch .LBB0_391

.LBB0_486:
	s_cmpk_lt_i32 s90, 0x80
	s_cselect_b64 s[8:9], -1, 0
	s_xor_b64 s[0:1], s[0:1], -1
	s_or_b64 s[0:1], s[8:9], s[0:1]
	s_and_b64 vcc, exec, s[0:1]
	s_cbranch_vccnz .LBB0_598
	s_lshl_b32 s14, s90, 3
	s_add_i32 s14, s14, s88
	s_add_i32 s17, s14, 0xfffffc00
	s_cmpk_gt_i32 s17, 0x29ff
	s_cbranch_scc1 .LBB0_598
	s_add_i32 s0, s17, 0x5800
	s_ashr_i32 s0, s0, 9
	s_and_b32 s15, s17, 0x1ff
	s_mul_i32 s16, s0, 0x300
	s_or_b32 s18, s15, 0x3000
	s_add_i32 s16, s16, s18
	s_cmpk_gt_i32 s16, 0x25ff
	s_cbranch_scc0 .LBB0_495
	s_cmpk_gt_u32 s16, 0x27ff
	s_cbranch_scc0 .LBB0_496
	s_cmpk_gt_u32 s16, 0x2bff
	s_cbranch_scc0 .LBB0_497
	s_cmpk_gt_u32 s16, 0x2fff
	s_cbranch_scc0 .LBB0_498
	s_add_i32 s19, s16, 0xffffd000
	s_and_b32 s0, s19, 0xffff
	s_mul_i32 s0, s0, 0xaaab
	s_lshr_b32 s12, s0, 25
	s_mul_i32 s0, s12, 0x300
	s_sub_i32 s0, s19, s0
	s_and_b32 s13, s0, 0xffff
	s_cmpk_gt_u32 s13, 0x1ff
	s_cbranch_scc0 .LBB0_499
	s_cmpk_gt_u32 s19, 0xbfff
	s_cbranch_scc0 .LBB0_500
	s_add_i32 s0, 0, 0x27ea8
	s_waitcnt vmcnt(15)
	v_mov_b32_e32 v2, s0
	ds_read_b64 v[2:3], v2
	s_mov_b64 s[8:9], 0
	s_waitcnt lgkmcnt(0)
	v_readfirstlane_b32 s0, v2
	v_readfirstlane_b32 s1, v3
	s_branch .LBB0_501

.LBB0_524:
	v_lshrrev_b32_e32 v131, 4, v196
	s_waitcnt vmcnt(15)
	v_mul_u32_u24_e32 v2, s10, v131
	v_and_b32_e32 v130, 60, v204
	v_mov_b32_e32 v133, 0
	s_waitcnt lgkmcnt(0)
	v_lshlrev_b32_e32 v132, 2, v2
	v_lshl_add_u64 v[2:3], s[8:9], 0, v[132:133]
	v_lshlrev_b32_e32 v132, 2, v130
	v_or_b32_e32 v135, 4, v131
	s_waitcnt vmcnt(13)
	v_lshl_add_u64 v[10:11], v[2:3], 0, v[132:133]
	v_mul_u32_u24_e32 v2, s10, v135
	v_lshlrev_b32_e32 v2, 2, v2
	v_mov_b32_e32 v3, v133
	v_lshl_add_u64 v[2:3], s[8:9], 0, v[2:3]
	v_or_b32_e32 v139, 8, v131
	v_lshl_add_u64 v[12:13], v[2:3], 0, v[132:133]
	global_load_dwordx4 v[2:5], v[10:11], off nt
	global_load_dwordx4 v[6:9], v[12:13], off nt
	v_mul_u32_u24_e32 v10, s10, v139
	v_lshlrev_b32_e32 v10, 2, v10
	v_mov_b32_e32 v11, v133
	v_lshl_add_u64 v[10:11], s[8:9], 0, v[10:11]
	v_or_b32_e32 v141, 12, v131
	s_waitcnt vmcnt(13)
	v_lshl_add_u64 v[18:19], v[10:11], 0, v[132:133]
	v_mul_u32_u24_e32 v10, s10, v141
	v_lshlrev_b32_e32 v10, 2, v10
	v_mov_b32_e32 v11, v133
	v_lshl_add_u64 v[10:11], s[8:9], 0, v[10:11]
	v_or_b32_e32 v143, 16, v131
	v_lshl_add_u64 v[20:21], v[10:11], 0, v[132:133]
	global_load_dwordx4 v[10:13], v[18:19], off nt
	global_load_dwordx4 v[14:17], v[20:21], off nt
	v_mul_u32_u24_e32 v18, s10, v143
	v_lshlrev_b32_e32 v18, 2, v18
	v_mov_b32_e32 v19, v133
	v_lshl_add_u64 v[18:19], s[8:9], 0, v[18:19]
	v_or_b32_e32 v145, 20, v131
	s_waitcnt vmcnt(13)
	v_lshl_add_u64 v[26:27], v[18:19], 0, v[132:133]
	v_mul_u32_u24_e32 v18, s10, v145
	v_lshlrev_b32_e32 v18, 2, v18
	v_mov_b32_e32 v19, v133
	v_lshl_add_u64 v[18:19], s[8:9], 0, v[18:19]
	v_or_b32_e32 v147, 24, v131
	v_lshl_add_u64 v[28:29], v[18:19], 0, v[132:133]
	global_load_dwordx4 v[18:21], v[26:27], off nt
	global_load_dwordx4 v[22:25], v[28:29], off nt
	v_mul_u32_u24_e32 v26, s10, v147
	v_lshlrev_b32_e32 v26, 2, v26
	v_mov_b32_e32 v27, v133
	v_lshl_add_u64 v[26:27], s[8:9], 0, v[26:27]
	v_or_b32_e32 v149, 28, v131
	s_waitcnt vmcnt(13)
	v_lshl_add_u64 v[34:35], v[26:27], 0, v[132:133]
	v_mul_u32_u24_e32 v26, s10, v149
	v_lshlrev_b32_e32 v26, 2, v26
	v_mov_b32_e32 v27, v133
	v_lshl_add_u64 v[26:27], s[8:9], 0, v[26:27]
	v_or_b32_e32 v151, 32, v131
	v_lshl_add_u64 v[36:37], v[26:27], 0, v[132:133]
	global_load_dwordx4 v[26:29], v[34:35], off nt
	global_load_dwordx4 v[30:33], v[36:37], off nt
	v_mul_u32_u24_e32 v34, s10, v151
	v_lshlrev_b32_e32 v34, 2, v34
	v_mov_b32_e32 v35, v133
	v_lshl_add_u64 v[34:35], s[8:9], 0, v[34:35]
	v_or_b32_e32 v163, 36, v131
	s_waitcnt vmcnt(13)
	v_lshl_add_u64 v[42:43], v[34:35], 0, v[132:133]
	v_mul_u32_u24_e32 v34, s10, v163
	v_lshlrev_b32_e32 v34, 2, v34
	v_mov_b32_e32 v35, v133
	v_lshl_add_u64 v[34:35], s[8:9], 0, v[34:35]
	v_or_b32_e32 v165, 40, v131
	v_lshl_add_u64 v[44:45], v[34:35], 0, v[132:133]
	global_load_dwordx4 v[34:37], v[42:43], off nt
	global_load_dwordx4 v[38:41], v[44:45], off nt
	v_mul_u32_u24_e32 v42, s10, v165
	v_lshlrev_b32_e32 v42, 2, v42
	v_mov_b32_e32 v43, v133
	v_lshl_add_u64 v[42:43], s[8:9], 0, v[42:43]
	v_or_b32_e32 v167, 44, v131
	s_waitcnt vmcnt(13)
	v_lshl_add_u64 v[50:51], v[42:43], 0, v[132:133]
	v_mul_u32_u24_e32 v42, s10, v167
	v_lshlrev_b32_e32 v42, 2, v42
	v_mov_b32_e32 v43, v133
	v_lshl_add_u64 v[42:43], s[8:9], 0, v[42:43]
	v_or_b32_e32 v169, 48, v131
	v_lshl_add_u64 v[52:53], v[42:43], 0, v[132:133]
	global_load_dwordx4 v[42:45], v[50:51], off nt
	global_load_dwordx4 v[46:49], v[52:53], off nt
	v_mul_u32_u24_e32 v50, s10, v169
	v_lshlrev_b32_e32 v50, 2, v50
	v_mov_b32_e32 v51, v133
	v_lshl_add_u64 v[50:51], s[8:9], 0, v[50:51]
	v_or_b32_e32 v171, 52, v131
	v_lshl_add_u64 v[58:59], v[50:51], 0, v[132:133]
	v_mul_u32_u24_e32 v50, s10, v171
	v_lshlrev_b32_e32 v50, 2, v50
	v_mov_b32_e32 v51, v133
	v_lshl_add_u64 v[50:51], s[8:9], 0, v[50:51]
	v_or_b32_e32 v180, 56, v131
	v_lshl_add_u64 v[60:61], v[50:51], 0, v[132:133]
	global_load_dwordx4 v[50:53], v[58:59], off nt
	global_load_dwordx4 v[54:57], v[60:61], off nt
	v_mul_u32_u24_e32 v58, s10, v180
	v_or_b32_e32 v181, 60, v131
	v_lshlrev_b32_e32 v58, 2, v58
	v_mov_b32_e32 v59, v133
	v_mul_u32_u24_e32 v60, s10, v181
	v_lshl_add_u64 v[58:59], s[8:9], 0, v[58:59]
	v_lshlrev_b32_e32 v60, 2, v60
	v_mov_b32_e32 v61, v133
	v_lshl_add_u64 v[58:59], v[58:59], 0, v[132:133]
	v_lshl_add_u64 v[60:61], s[8:9], 0, v[60:61]
	v_lshl_add_u64 v[60:61], v[60:61], 0, v[132:133]
	global_load_dwordx4 v[74:77], v[58:59], off nt
	global_load_dwordx4 v[78:81], v[60:61], off nt
	s_lshl_b32 s8, s15, 5
	s_and_b32 s22, s8, 0xc0
	s_lshl_b32 s8, s15, 6
	s_bfe_u32 s21, s87, 0x10006
	s_and_b32 s23, s8, 64
	s_add_u32 s25, s50, 0x14400000
	s_addc_u32 s26, s51, 0
	s_add_u32 s27, s50, 0x4000000
	s_addc_u32 s28, s51, 0
	s_add_u32 s29, s50, 0x1600000
	s_addc_u32 s30, s51, 0
	s_add_u32 s31, s50, 0xe00000
	s_addc_u32 s33, s51, 0
	v_and_b32_e32 v60, 7, v0
	v_lshrrev_b32_e32 v134, 3, v196
	v_add_u32_e32 v58, s20, v132
	v_mul_u32_u24_e32 v59, 0x104, v131
	s_add_u32 s34, s50, 0xa00000
	v_mul_u32_u24_e32 v61, 0x820, v60
	v_lshlrev_b32_e32 v62, 2, v134
	s_addc_u32 s35, s51, 0
	v_lshlrev_b32_e32 v136, 3, v60
	v_mov_b32_e32 v137, v133
	v_add3_u32 v182, s20, v61, v62
	v_or_b32_e32 v138, 8, v134
	v_or_b32_e32 v140, 16, v134
	v_or_b32_e32 v142, 24, v134
	v_or_b32_e32 v144, 32, v134
	v_or_b32_e32 v146, 40, v134
	v_or_b32_e32 v148, 48, v134
	v_or_b32_e32 v150, 56, v134
	v_lshlrev_b32_e32 v152, 4, v60
	v_mov_b32_e32 v153, v133
	s_add_i32 s57, s14, 0x4c00
	s_add_i32 s20, 0, 0x27ea8
	s_add_i32 s37, 0, 0x27e90
	s_movk_i32 s42, 0x98
	s_movk_i32 s43, 0x88
	s_add_i32 s44, 0, 0x27e60
	s_add_i32 s45, 0, 0x27e58
	s_add_i32 s46, 0, 0x27e50
	s_add_i32 s47, 0, 0x27e30
	s_mov_b32 s53, 0xc3e00000
	v_add_u32_e32 v183, v58, v59
	v_mov_b32_e32 v184, 0x43e00000
	s_mov_b32 s56, s24
	s_mov_b32 s55, s19
	s_mov_b64 s[8:9], s[0:1]
	s_branch .LBB0_528
